# MLA spread schedule with 5 deferred exps in front of the first QK MFMA (covers the fragment read latency after the barrier)
# baseline (speedup 1.0000x reference)
; #define LAS __attribute__((address_space(3)))
; DEV float ex2(float x) { return __builtin_amdgcn_exp2f(x); }
; #define MLA_SB() __builtin_amdgcn_sched_barrier(0)
; #define MLA_PIN(x) asm volatile("" : "+v"(x))
; #define MFMA8(a, b, c) __builtin_amdgcn_mfma_scale_f32_32x32x64_f8f6f4((a), (b), (c), 0, 0, 0, 0x7f7f7f7f, 0, 0x7c7c7c7c)
; #define MFMA8PV(a, b, c) __builtin_amdgcn_mfma_scale_f32_32x32x64_f8f6f4((a), (b), (c), 0, 1, 0, 0x7f7f7f7f, 0, 0x7f7f7f7f)
; DEV unsigned pk_bf8x4(float a, float b, float c, float d, int old = 0) { int w = __builtin_amdgcn_cvt_pk_bf8_f32(a, b, old, false); w = __builtin_amdgcn_cvt_pk_bf8_f32(c, d, w, true); return (unsigned)w; }
; template <int VAR> DEV void mla_step(f32x16& C0, f32x16& C1, f32x16& P0, f32x16& P1, f32x16& o0, f32x16& o1, f32x16& lacc,
;                   const v8i (&qf)[2], const f32x16& cini, LAS char* kp, LAS char* vp, v8i& pw) {
;     v8i kf[2], vf[2];
;     const v8i ones8 = {0x38383838, 0x38383838, 0x38383838, 0x38383838, 0x38383838, 0x38383838, 0x38383838, 0x38383838};
;     kf[0] = mla_kf8(kp, 0, 0); kf[1] = mla_kf8(kp, 1, 0);
;     MLA_SB();
; #pragma unroll
;     for (int g = 0; g < 4; ++g) {
;         const int kb = g & 1, sx = g >> 1;
;         if (kb) C1 = MFMA8(kf[1], qf[sx], sx == 0 ? cini : C1); else C0 = MFMA8(kf[0], qf[sx], sx == 0 ? cini : C0);
;         if (g < 2) kf[kb] = mla_kf8(kp, kb, 1);
;         if (g >= 2) vf[g - 2] = mla_vf8(vp, g - 2);
; #pragma unroll
;         for (int j = 0; j < 2; ++j) { const int w = 2 * g + j, e = 4 * w;
;             if (VAR == 3) pw[w] = __builtin_bit_cast(int, (e < 16) ? P0[e] : P1[e - 16]);
;             else pw[w] = (int)((e < 16) ? pk_bf8x4(P0[e], P0[e + 1], P0[e + 2], P0[e + 3], pw[w]) : pk_bf8x4(P1[e - 16], P1[e - 15], P1[e - 14], P1[e - 13], pw[w])); }
;         if (g == 3) MLA_PIN(pw);
;         MLA_SB();
;     }
; #pragma unroll
;     for (int g = 0; g < 3; ++g) {
;         if (g == 0) o0 = MFMA8PV(vf[0], pw, o0); else if (g == 1) o1 = MFMA8PV(vf[1], pw, o1); else lacc = MFMA8PV(ones8, pw, lacc);
;         const int e0 = (g * 32) / 3, e1 = ((g + 1) * 32) / 3;
; #pragma unroll
;         for (int e = e0; e < e1; ++e) { if (VAR == 2 || VAR == 3) continue; if (e < 16) C0[e] = ex2(C0[e]); else C1[e - 16] = ex2(C1[e - 16]); }
;         if (g < 2) MLA_PIN(C0);
;         if (g > 0) MLA_PIN(C1);
;         MLA_SB();
;     }
; }
.LBB0_812:
	s_mul_i32 s2, s62, 0x6000
	v_add_u32_e32 v172, s2, v200
	ds_read_b128 v[98:101], v172 offset:8192
	ds_read_b128 v[106:109], v172 offset:8704
	ds_read_b128 v[102:105], v172 offset:9216
	ds_read_b128 v[110:113], v172 offset:9728
	v_cvt_pk_bf8_f32 v146, v82, v83
	v_cvt_pk_bf8_f32 v147, v86, v87
	v_exp_f32_e32 v69, v69
	v_exp_f32_e32 v70, v70
	v_exp_f32_e32 v71, v71
	v_exp_f32_e32 v72, v72
	v_exp_f32_e32 v73, v73
	s_waitcnt lgkmcnt(1)
	v_mfma_scale_f32_32x32x64_f8f6f4 v[114:129], v[98:105], v[138:145], v[2:17], v209, v208 op_sel_hi:[0,0,0]
	ds_read_b128 v[154:157], v172 offset:12288
	ds_read_b128 v[158:161], v172 offset:13312
	v_cvt_pk_bf8_f32 v146, v84, v85 op_sel:[0,0,1]
	v_cvt_pk_bf8_f32 v147, v88, v89 op_sel:[0,0,1]
	v_cvt_pk_bf8_f32 v148, v90, v91
	v_cvt_pk_bf8_f32 v149, v94, v95
	ds_read_b128 v[82:85], v172 offset:12800
	ds_read_b128 v[86:89], v172 offset:13824
	v_exp_f32_e32 v74, v74
	v_exp_f32_e32 v75, v75
	s_waitcnt lgkmcnt(4)
	v_mfma_scale_f32_32x32x64_f8f6f4 v[98:113], v[106:113], v[138:145], v[2:17], v209, v208 op_sel_hi:[0,0,0]
	v_cvt_pk_bf8_f32 v148, v92, v93 op_sel:[0,0,1]
	v_cvt_pk_bf8_f32 v149, v96, v97 op_sel:[0,0,1]
	ds_read_b128 v[90:93], v172 offset:16384
	ds_read_b128 v[94:97], v172 offset:17408
	v_exp_f32_e32 v76, v76
	v_exp_f32_e32 v77, v77
	v_exp_f32_e32 v78, v78
	s_waitcnt lgkmcnt(4)
	v_mfma_scale_f32_32x32x64_f8f6f4 v[114:129], v[154:161], v[130:137], v[114:129], v209, v208 op_sel_hi:[0,0,0]
	v_exp_f32_e32 v79, v79
	v_exp_f32_e32 v80, v80
	v_exp_f32_e32 v81, v81
	s_waitcnt lgkmcnt(2)
	v_mfma_scale_f32_32x32x64_f8f6f4 v[98:113], v[82:89], v[130:137], v[98:113], v209, v208 op_sel_hi:[0,0,0]
	v_cvt_pk_bf8_f32 v150, v66, v67
	v_cvt_pk_bf8_f32 v151, v70, v71
	v_cvt_pk_bf8_f32 v150, v68, v69 op_sel:[0,0,1]
	v_cvt_pk_bf8_f32 v151, v72, v73 op_sel:[0,0,1]
	v_cvt_pk_bf8_f32 v152, v74, v75
	v_cvt_pk_bf8_f32 v153, v78, v79
	v_cvt_pk_bf8_f32 v152, v76, v77 op_sel:[0,0,1]
	v_cvt_pk_bf8_f32 v153, v80, v81 op_sel:[0,0,1]
	ds_read_b128 v[66:69], v172 offset:16896
	ds_read_b128 v[70:73], v172 offset:17920
	s_waitcnt lgkmcnt(2)
	v_mfma_scale_f32_32x32x64_f8f6f4 v[50:65], v[90:97], v[146:153], v[50:65], v209, v209 op_sel_hi:[0,0,0] blgp:1
	s_nop 2
	v_exp_f32_e32 v114, v114
	v_exp_f32_e32 v115, v115
	v_exp_f32_e32 v116, v116
	v_exp_f32_e32 v117, v117
	v_exp_f32_e32 v118, v118
	v_exp_f32_e32 v119, v119
	s_waitcnt lgkmcnt(0)
	v_mfma_scale_f32_32x32x64_f8f6f4 v[18:33], v[66:73], v[146:153], v[18:33], v209, v209 op_sel_hi:[0,0,0] blgp:1
	v_exp_f32_e32 v120, v120
	v_exp_f32_e32 v121, v121
	v_exp_f32_e32 v122, v122
	v_exp_f32_e32 v123, v123
	v_exp_f32_e32 v124, v124
	v_exp_f32_e32 v125, v125
	v_mfma_scale_f32_32x32x64_f8f6f4 v[34:49], v[210:217], v[146:153], v[34:49], v209, v209 op_sel_hi:[0,0,0] blgp:1
	v_exp_f32_e32 v126, v126
	v_exp_f32_e32 v127, v127
	v_exp_f32_e32 v128, v128
	v_exp_f32_e32 v129, v129
	v_exp_f32_e32 v98, v98
	v_exp_f32_e32 v99, v99
	v_exp_f32_e32 v100, v100
	s_add_i32 s61, s61, 1
	s_add_i32 s2, s62, 1
	s_cmp_lg_u32 s62, 2
	s_cselect_b32 s62, s2, 0
	s_mul_i32 s64, s62, 0x6000
	s_add_i32 s2, s64, 0x6000
	s_cmp_eq_u32 s62, 2
	s_cselect_b64 s[8:9], -1, 0
	s_cmp_eq_u32 s100, 0
	s_cbranch_scc1 .Lmla_w0
	s_cmp_eq_u32 s100, 1
	s_cbranch_scc1 .Lmla_w1
	s_waitcnt vmcnt(2)
	s_branch .Lmla_wd

; #define LAS __attribute__((address_space(3)))
; #define WAITV(n) asm volatile("s_waitcnt vmcnt(%0)" ::"n"(n) : "memory")
; DEV float ex2(float x) { return __builtin_amdgcn_exp2f(x); }
; #define MLA_SB() __builtin_amdgcn_sched_barrier(0)
; template <int VAR> DEV void mla_step(f32x16& C0, f32x16& C1, f32x16& P0, f32x16& P1, f32x16& o0, f32x16& o1, f32x16& lacc,
;                   const v8i (&qf)[2], const f32x16& cini, LAS char* kp, LAS char* vp, v8i& pw) {
;     v8i kf[2], vf[2];
;     const v8i ones8 = {0x38383838, 0x38383838, 0x38383838, 0x38383838, 0x38383838, 0x38383838, 0x38383838, 0x38383838};
;     kf[0] = mla_kf8(kp, 0, 0); kf[1] = mla_kf8(kp, 1, 0);
;     MLA_SB();
; #pragma unroll
;     for (int g = 0; g < 4; ++g) {
;         const int kb = g & 1, sx = g >> 1;
;         if (kb) C1 = MFMA8(kf[1], qf[sx], sx == 0 ? cini : C1); else C0 = MFMA8(kf[0], qf[sx], sx == 0 ? cini : C0);
;         if (g < 2) kf[kb] = mla_kf8(kp, kb, 1);
;         if (g >= 2) vf[g - 2] = mla_vf8(vp, g - 2);
; #pragma unroll
;         for (int j = 0; j < 2; ++j) { const int w = 2 * g + j, e = 4 * w;
;             if (VAR == 3) pw[w] = __builtin_bit_cast(int, (e < 16) ? P0[e] : P1[e - 16]);
;             else pw[w] = (int)((e < 16) ? pk_bf8x4(P0[e], P0[e + 1], P0[e + 2], P0[e + 3], pw[w]) : pk_bf8x4(P1[e - 16], P1[e - 15], P1[e - 14], P1[e - 13], pw[w])); }
;         if (g == 3) MLA_PIN(pw);
;         MLA_SB();
;     }
; #pragma unroll
;     for (int g = 0; g < 3; ++g) {
;         if (g == 0) o0 = MFMA8PV(vf[0], pw, o0); else if (g == 1) o1 = MFMA8PV(vf[1], pw, o1); else lacc = MFMA8PV(ones8, pw, lacc);
;         const int e0 = (g * 32) / 3, e1 = ((g + 1) * 32) / 3;
; #pragma unroll
;         for (int e = e0; e < e1; ++e) { if (VAR == 2 || VAR == 3) continue; if (e < 16) C0[e] = ex2(C0[e]); else C1[e - 16] = ex2(C1[e - 16]); }
;         if (g < 2) MLA_PIN(C0);
;         if (g > 0) MLA_PIN(C1);
;         MLA_SB();
;     }
; }
; template <int VAR> DEV void mla_unit(const Params& p, int layer, int b, int hd, int tokbase, int t0, int t1, LAS char* lds, SideJob& sj) {
;     ...
;             WAITV(0); SBAR();
;             if (s + 2 < ns) MLA_ISSUE(t0 + s + 2, (nslot == 2) ? 0 : nslot + 1);
;             { LAS char* nb = lds + nslot * STG; LAS char* ob = lds + slot * STG; mla_step<VAR>(sA0, sA1, sB0, sB1, o0, o1, lacc, qf, cini, nb + koffl, ob + MLA_VSUB + voffl, pw); }
.Lmla_wd:
	s_and_b64 s[20:21], s[8:9], exec
	s_waitcnt lgkmcnt(0)
	s_barrier
	s_cselect_b32 s2, 0, s2
	s_add_i32 s2, s2, s60
	s_mov_b32 s3, m0
	s_mov_b32 m0, s2
	v_add_u32_e32 v173, s64, v200
	ds_read_b128 v[66:69], v173
	ds_read_b128 v[74:77], v173 offset:512
	ds_read_b128 v[70:73], v173 offset:1024
	ds_read_b128 v[78:81], v173 offset:1536
	v_cvt_pk_bf8_f32 v146, v114, v115
	v_cvt_pk_bf8_f32 v147, v118, v119
	v_exp_f32_e32 v101, v101
	v_exp_f32_e32 v102, v102
	v_exp_f32_e32 v103, v103
	v_exp_f32_e32 v104, v104
	v_exp_f32_e32 v105, v105
	s_waitcnt lgkmcnt(1)
	v_mfma_scale_f32_32x32x64_f8f6f4 v[82:97], v[66:73], v[138:145], v[2:17], v209, v208 op_sel_hi:[0,0,0]
	global_load_lds_dwordx4 v[162:163], off
	ds_read_b128 v[164:167], v173 offset:4096
	ds_read_b128 v[168:171], v173 offset:5120
	v_cvt_pk_bf8_f32 v146, v116, v117 op_sel:[0,0,1]
	v_cvt_pk_bf8_f32 v147, v120, v121 op_sel:[0,0,1]
	v_cvt_pk_bf8_f32 v148, v122, v123
	v_cvt_pk_bf8_f32 v149, v126, v127
	ds_read_b128 v[114:117], v173 offset:4608
	ds_read_b128 v[118:121], v173 offset:5632
	v_exp_f32_e32 v106, v106
	v_exp_f32_e32 v107, v107
	s_waitcnt lgkmcnt(4)
	v_mfma_scale_f32_32x32x64_f8f6f4 v[66:81], v[74:81], v[138:145], v[2:17], v209, v208 op_sel_hi:[0,0,0]
	global_load_lds_dwordx4 v[162:163], off offset:1024
	v_cvt_pk_bf8_f32 v148, v124, v125 op_sel:[0,0,1]
	v_cvt_pk_bf8_f32 v149, v128, v129 op_sel:[0,0,1]
	ds_read_b128 v[122:125], v172 offset:20480
	ds_read_b128 v[126:129], v172 offset:21504
	v_exp_f32_e32 v108, v108
	v_exp_f32_e32 v109, v109
	v_exp_f32_e32 v110, v110
	s_waitcnt lgkmcnt(4)
	v_mfma_scale_f32_32x32x64_f8f6f4 v[82:97], v[164:171], v[130:137], v[82:97], v209, v208 op_sel_hi:[0,0,0]
	global_load_lds_dwordx4 v[162:163], off offset:2048
	s_mov_b32 m0, s3
	v_exp_f32_e32 v111, v111
	v_exp_f32_e32 v112, v112
	v_exp_f32_e32 v113, v113
	s_waitcnt lgkmcnt(2)
	v_mfma_scale_f32_32x32x64_f8f6f4 v[66:81], v[114:121], v[130:137], v[66:81], v209, v208 op_sel_hi:[0,0,0]
	v_cvt_pk_bf8_f32 v150, v98, v99
	v_cvt_pk_bf8_f32 v151, v102, v103
	v_cvt_pk_bf8_f32 v150, v100, v101 op_sel:[0,0,1]
	v_cvt_pk_bf8_f32 v151, v104, v105 op_sel:[0,0,1]
	v_cvt_pk_bf8_f32 v152, v106, v107
	v_cvt_pk_bf8_f32 v153, v110, v111
	v_cvt_pk_bf8_f32 v152, v108, v109 op_sel:[0,0,1]
	v_cvt_pk_bf8_f32 v153, v112, v113 op_sel:[0,0,1]
	ds_read_b128 v[98:101], v172 offset:20992
	ds_read_b128 v[102:105], v172 offset:22016
	s_waitcnt lgkmcnt(2)
	v_mfma_scale_f32_32x32x64_f8f6f4 v[50:65], v[122:129], v[146:153], v[50:65], v209, v209 op_sel_hi:[0,0,0] blgp:1
	s_nop 2
	v_exp_f32_e32 v82, v82
	v_exp_f32_e32 v83, v83
	v_exp_f32_e32 v84, v84
	v_exp_f32_e32 v85, v85
	v_exp_f32_e32 v86, v86
	v_exp_f32_e32 v87, v87
	s_waitcnt lgkmcnt(0)
	v_mfma_scale_f32_32x32x64_f8f6f4 v[18:33], v[98:105], v[146:153], v[18:33], v209, v209 op_sel_hi:[0,0,0] blgp:1
	v_exp_f32_e32 v88, v88
	v_exp_f32_e32 v89, v89
	v_exp_f32_e32 v90, v90
	v_exp_f32_e32 v91, v91
	v_exp_f32_e32 v92, v92
	v_exp_f32_e32 v93, v93
	v_mfma_scale_f32_32x32x64_f8f6f4 v[34:49], v[210:217], v[146:153], v[34:49], v209, v209 op_sel_hi:[0,0,0] blgp:1
	v_exp_f32_e32 v94, v94
	v_exp_f32_e32 v95, v95
	v_exp_f32_e32 v96, v96
	v_exp_f32_e32 v97, v97
	v_exp_f32_e32 v66, v66
	v_exp_f32_e32 v67, v67
	v_exp_f32_e32 v68, v68
	s_mov_b64 s[20:21], 0x6000
	s_cmpk_lg_i32 s61, 0x80
	v_lshl_add_u64 v[162:163], v[162:163], 0, s[20:21]
	s_cbranch_scc0 .LBB0_835
